# PREP queue fetches: store-drain wait before the index atomic removed (atomic round trip overlaps the drain), on top of v84
# speedup vs baseline: 1.0093x; 1.0013x over previous
.LBB0_257:
	s_waitcnt lgkmcnt(0)
	s_barrier
	s_and_saveexec_b64 s[0:1], s[36:37]
	s_cbranch_execz .LBB0_259
	v_mov_b64_e32 v[4:5], s[8:9]
	global_atomic_add v1, v[4:5], v228, off sc0
	v_mov_b32_e32 v2, s23
	s_waitcnt vmcnt(0) lgkmcnt(0)
	ds_write_b32 v2, v1

.LBB0_379:
	s_waitcnt lgkmcnt(0)
	s_barrier
	s_and_saveexec_b64 s[8:9], s[0:1]
	s_cbranch_execz .LBB0_381
	v_mov_b64_e32 v[4:5], s[4:5]
	global_atomic_add v1, v[4:5], v228, off sc0
	v_mov_b32_e32 v2, s2
	s_waitcnt vmcnt(0) lgkmcnt(0)
	ds_write_b32 v2, v1

.LBB0_386:
	s_waitcnt lgkmcnt(0)
	s_barrier
	s_and_saveexec_b64 s[4:5], s[36:37]
	s_cbranch_execz .LBB0_388
	v_mov_b64_e32 v[4:5], s[0:1]
	global_atomic_add v1, v[4:5], v228, off sc0
	v_mov_b32_e32 v2, s2
	s_waitcnt vmcnt(0) lgkmcnt(0)
	ds_write_b32 v2, v1

.LBB0_396:
	s_barrier
	s_and_saveexec_b64 s[0:1], s[36:37]
	s_cbranch_execz .LBB0_398
	v_mov_b64_e32 v[4:5], s[4:5]
	global_atomic_add v1, v[4:5], v228, off sc0
	v_mov_b32_e32 v2, s2
	s_waitcnt vmcnt(0) lgkmcnt(0)
	ds_write_b32 v2, v1
